# xnorm prologue: the 16 w_in column loads of the four k-iterations issued together instead of four serial load-convert-write rounds
# speedup vs baseline: 1.0072x; 1.0070x over previous
; DI bf16_t f2bf(float x) { return (bf16_t)(pk2(x, 0.f) & 0xffffu); }
; DI void phase_xnorm(const Params& p, int bid, int nb, char* lds) {
;     ...
;   __syncthreads();
;   for (int k = tid; k < 1024; k += NT) {
;     const float* src = p.w_in + (size_t)k * 5648;
;     const f32x4 w0 = *(const f32x4*)(src + 1536), w1 = *(const f32x4*)(src + 1540), w2 = *(const f32x4*)(src + 3592), w3 = *(const f32x4*)(src + 3596);
; #pragma unroll
;     for (int e = 0; e < 4; ++e) { *(bf16_t*)(w16 + e * WP + 2 * k) = f2bf(w0[e]); *(bf16_t*)(w16 + (4 + e) * WP + 2 * k) = f2bf(w1[e]);
;       *(bf16_t*)(w16 + (8 + e) * WP + 2 * k) = f2bf(w2[e]); *(bf16_t*)(w16 + (12 + e) * WP + 2 * k) = f2bf(w3[e]); }
;   }
.LBB0_87:
	s_or_b64 exec, exec, s[0:1]
	v_mov_b32_e32 v2, v206
	s_movk_i32 s0, 0x400
	s_waitcnt lgkmcnt(0)
	s_barrier
	s_nop 0
	v_cmp_gt_i32_e32 vcc, s0, v2
	s_barrier
	s_and_saveexec_b64 s[0:1], vcc
	s_cbranch_execz .LBB0_90
	v_lshlrev_b32_e32 v0, 1, v2
	v_add3_u32 v4, v190, v0, 0
	s_movk_i32 s2, 0x5840
	v_mov_b64_e32 v[0:1], s[48:49]
	v_mad_i64_i32 v[0:1], s[2:3], v2, s2, v[0:1]
	s_mov_b64 s[2:3], 0x3820
	s_movk_i32 s6, 0xdfe0
	v_add_u32_e32 v3, 0xffffff00, v2
	v_lshl_add_u64 v[0:1], v[0:1], 0, s[2:3]
	s_mov_b64 s[4:5], 0
	s_mov_b32 s7, -1
	s_mov_b64 s[8:9], 0x584000
	s_movk_i32 s2, 0x2ff
	v_lshl_add_u64 v[88:89], v[0:1], 0, s[8:9]
	v_lshl_add_u64 v[90:91], v[88:89], 0, s[8:9]
	v_lshl_add_u64 v[92:93], v[90:91], 0, s[8:9]
	v_lshl_add_u64 v[94:95], v[0:1], 0, s[6:7]
	v_lshl_add_u64 v[96:97], v[88:89], 0, s[6:7]
	v_lshl_add_u64 v[98:99], v[90:91], 0, s[6:7]
	v_lshl_add_u64 v[100:101], v[92:93], 0, s[6:7]
	global_load_dwordx4 v[24:27], v[0:1], off
	global_load_dwordx4 v[28:31], v[0:1], off offset:16
	global_load_dwordx4 v[32:35], v[94:95], off
	global_load_dwordx4 v[36:39], v[94:95], off offset:16
	global_load_dwordx4 v[40:43], v[88:89], off
	global_load_dwordx4 v[44:47], v[88:89], off offset:16
	global_load_dwordx4 v[48:51], v[96:97], off
	global_load_dwordx4 v[52:55], v[96:97], off offset:16
	global_load_dwordx4 v[56:59], v[90:91], off
	global_load_dwordx4 v[60:63], v[90:91], off offset:16
	global_load_dwordx4 v[64:67], v[98:99], off
	global_load_dwordx4 v[68:71], v[98:99], off offset:16
	global_load_dwordx4 v[72:75], v[92:93], off
	global_load_dwordx4 v[76:79], v[92:93], off offset:16
	global_load_dwordx4 v[80:83], v[100:101], off
	global_load_dwordx4 v[84:87], v[100:101], off offset:16
	s_waitcnt vmcnt(12)
	v_cvt_pk_bf16_f32 v102, v24, s0
	v_cvt_pk_bf16_f32 v103, v25, s0
	v_cvt_pk_bf16_f32 v104, v26, s0
	v_cvt_pk_bf16_f32 v105, v27, s0
	v_cvt_pk_bf16_f32 v106, v28, s0
	v_cvt_pk_bf16_f32 v107, v29, s0
	v_cvt_pk_bf16_f32 v108, v30, s0
	v_cvt_pk_bf16_f32 v109, v31, s0
	v_cvt_pk_bf16_f32 v110, v32, s0
	v_cvt_pk_bf16_f32 v111, v33, s0
	v_cvt_pk_bf16_f32 v112, v34, s0
	v_cvt_pk_bf16_f32 v113, v35, s0
	v_cvt_pk_bf16_f32 v114, v36, s0
	v_cvt_pk_bf16_f32 v115, v37, s0
	v_cvt_pk_bf16_f32 v116, v38, s0
	v_cvt_pk_bf16_f32 v117, v39, s0
	ds_write_b16 v4, v102 offset:16512
	ds_write_b16 v4, v106 offset:24768
	ds_write_b16 v4, v103 offset:18576
	ds_write_b16 v4, v107 offset:26832
	ds_write_b16 v4, v104 offset:20640
	ds_write_b16 v4, v108 offset:28896
	ds_write_b16 v4, v105 offset:22704
	ds_write_b16 v4, v109 offset:30960
	ds_write_b16 v4, v110 offset:0
	ds_write_b16 v4, v114 offset:8256
	ds_write_b16 v4, v111 offset:2064
	ds_write_b16 v4, v115 offset:10320
	ds_write_b16 v4, v112 offset:4128
	ds_write_b16 v4, v116 offset:12384
	ds_write_b16 v4, v113 offset:6192
	ds_write_b16 v4, v117 offset:14448
	s_waitcnt vmcnt(8)
	v_cvt_pk_bf16_f32 v102, v40, s0
	v_cvt_pk_bf16_f32 v103, v41, s0
	v_cvt_pk_bf16_f32 v104, v42, s0
	v_cvt_pk_bf16_f32 v105, v43, s0
	v_cvt_pk_bf16_f32 v106, v44, s0
	v_cvt_pk_bf16_f32 v107, v45, s0
	v_cvt_pk_bf16_f32 v108, v46, s0
	v_cvt_pk_bf16_f32 v109, v47, s0
	v_cvt_pk_bf16_f32 v110, v48, s0
	v_cvt_pk_bf16_f32 v111, v49, s0
	v_cvt_pk_bf16_f32 v112, v50, s0
	v_cvt_pk_bf16_f32 v113, v51, s0
	v_cvt_pk_bf16_f32 v114, v52, s0
	v_cvt_pk_bf16_f32 v115, v53, s0
	v_cvt_pk_bf16_f32 v116, v54, s0
	v_cvt_pk_bf16_f32 v117, v55, s0
	ds_write_b16 v4, v102 offset:17024
	ds_write_b16 v4, v106 offset:25280
	ds_write_b16 v4, v103 offset:19088
	ds_write_b16 v4, v107 offset:27344
	ds_write_b16 v4, v104 offset:21152
	ds_write_b16 v4, v108 offset:29408
	ds_write_b16 v4, v105 offset:23216
	ds_write_b16 v4, v109 offset:31472
	ds_write_b16 v4, v110 offset:512
	ds_write_b16 v4, v114 offset:8768
	ds_write_b16 v4, v111 offset:2576
	ds_write_b16 v4, v115 offset:10832
	ds_write_b16 v4, v112 offset:4640
	ds_write_b16 v4, v116 offset:12896
	ds_write_b16 v4, v113 offset:6704
	ds_write_b16 v4, v117 offset:14960
	s_waitcnt vmcnt(4)
	v_cvt_pk_bf16_f32 v102, v56, s0
	v_cvt_pk_bf16_f32 v103, v57, s0
	v_cvt_pk_bf16_f32 v104, v58, s0
	v_cvt_pk_bf16_f32 v105, v59, s0
	v_cvt_pk_bf16_f32 v106, v60, s0
	v_cvt_pk_bf16_f32 v107, v61, s0
	v_cvt_pk_bf16_f32 v108, v62, s0
	v_cvt_pk_bf16_f32 v109, v63, s0
	v_cvt_pk_bf16_f32 v110, v64, s0
	v_cvt_pk_bf16_f32 v111, v65, s0
	v_cvt_pk_bf16_f32 v112, v66, s0
	v_cvt_pk_bf16_f32 v113, v67, s0
	v_cvt_pk_bf16_f32 v114, v68, s0
	v_cvt_pk_bf16_f32 v115, v69, s0
	v_cvt_pk_bf16_f32 v116, v70, s0
	v_cvt_pk_bf16_f32 v117, v71, s0
	ds_write_b16 v4, v102 offset:17536
	ds_write_b16 v4, v106 offset:25792
	ds_write_b16 v4, v103 offset:19600
	ds_write_b16 v4, v107 offset:27856
	ds_write_b16 v4, v104 offset:21664
	ds_write_b16 v4, v108 offset:29920
	ds_write_b16 v4, v105 offset:23728
	ds_write_b16 v4, v109 offset:31984
	ds_write_b16 v4, v110 offset:1024
	ds_write_b16 v4, v114 offset:9280
	ds_write_b16 v4, v111 offset:3088
	ds_write_b16 v4, v115 offset:11344
	ds_write_b16 v4, v112 offset:5152
	ds_write_b16 v4, v116 offset:13408
	ds_write_b16 v4, v113 offset:7216
	ds_write_b16 v4, v117 offset:15472
	s_waitcnt vmcnt(0)
	v_cvt_pk_bf16_f32 v102, v72, s0
	v_cvt_pk_bf16_f32 v103, v73, s0
	v_cvt_pk_bf16_f32 v104, v74, s0
	v_cvt_pk_bf16_f32 v105, v75, s0
	v_cvt_pk_bf16_f32 v106, v76, s0
	v_cvt_pk_bf16_f32 v107, v77, s0
	v_cvt_pk_bf16_f32 v108, v78, s0
	v_cvt_pk_bf16_f32 v109, v79, s0
	v_cvt_pk_bf16_f32 v110, v80, s0
	v_cvt_pk_bf16_f32 v111, v81, s0
	v_cvt_pk_bf16_f32 v112, v82, s0
	v_cvt_pk_bf16_f32 v113, v83, s0
	v_cvt_pk_bf16_f32 v114, v84, s0
	v_cvt_pk_bf16_f32 v115, v85, s0
	v_cvt_pk_bf16_f32 v116, v86, s0
	v_cvt_pk_bf16_f32 v117, v87, s0
	ds_write_b16 v4, v102 offset:18048
	ds_write_b16 v4, v106 offset:26304
	ds_write_b16 v4, v103 offset:20112
	ds_write_b16 v4, v107 offset:28368
	ds_write_b16 v4, v104 offset:22176
	ds_write_b16 v4, v108 offset:30432
	ds_write_b16 v4, v105 offset:24240
	ds_write_b16 v4, v109 offset:32496
	ds_write_b16 v4, v110 offset:1536
	ds_write_b16 v4, v114 offset:9792
	ds_write_b16 v4, v111 offset:3600
	ds_write_b16 v4, v115 offset:11856
	ds_write_b16 v4, v112 offset:5664
	ds_write_b16 v4, v116 offset:13920
	ds_write_b16 v4, v113 offset:7728
	ds_write_b16 v4, v117 offset:15984
